# v043 + XCD leaders also keep two staggered polls of the release word in flight
# baseline (speedup 1.0000x reference)
; __device__ __forceinline__ unsigned xb_ld(unsigned* p)              { return __hip_atomic_load(p, __ATOMIC_RELAXED, __HIP_MEMORY_SCOPE_AGENT); }
; __device__ __forceinline__ unsigned xb_add(unsigned* p, unsigned v) { return __hip_atomic_fetch_add(p, v, __ATOMIC_RELAXED, __HIP_MEMORY_SCOPE_AGENT); }
; #define XB_SPIN(cond, bar) do { unsigned _sp = 0; while (cond) { __builtin_amdgcn_s_sleep(1); \
;     if ((++_sp & 255u) == 0u) { if (xb_ld(&(bar)[XB_TMO])) break; if (_sp > XB_SPIN_CAP) { atomicAdd(&(bar)[XB_TMO], 1u); break; } } } } while (0)
; __device__ __forceinline__ void xcd_barrier(const XcdBarrier& b) {
;     ...
;         if (old + 1u == (gen + 1u) * nloc) {
;             __builtin_amdgcn_fence(__ATOMIC_RELEASE, "agent");
;             asm volatile("s_waitcnt vmcnt(0)" ::: "memory");
;             const unsigned og = xb_add(&bar[XB_TOP], 1u);
;             const unsigned tg = og / nx;
;             if (og + 1u == (tg + 1u) * nx) xb_add(&bar[XB_TOPGEN], 1u);
;             else XB_SPIN(xb_ld(&bar[XB_TOPGEN]) == tg, bar);
.LBB0_315:
	s_andn2_saveexec_b64 s[6:7], s[6:7]
	s_cbranch_execz .LBB0_335
	s_mov_b64 s[6:7], exec
	buffer_wbl2 sc1
	v_readlane_b32 s18, v253, 48
	v_readlane_b32 s19, v253, 49
	v_readlane_b32 s12, v253, 52
	v_readlane_b32 s13, v253, 53
	s_nop 3
	s_add_u32 s18, s18, 0x3600
	s_addc_u32 s19, s19, 0
	s_add_u32 s12, s12, 0x2500
	s_addc_u32 s13, s13, 0
	s_waitcnt lgkmcnt(0)
	s_waitcnt vmcnt(0)
	global_atomic_add v163, v197, s[12:13]
	global_atomic_add v163, v197, s[12:13] offset:256
	global_atomic_add v163, v197, s[12:13] offset:512
	global_atomic_add v163, v197, s[12:13] offset:768
	global_atomic_add v163, v197, s[12:13] offset:1024
	global_atomic_add v163, v197, s[12:13] offset:1280
	global_atomic_add v163, v197, s[12:13] offset:1536
	global_atomic_add v163, v197, s[12:13] offset:1792
	global_atomic_add v163, v197, s[12:13] offset:2048
	global_atomic_add v163, v197, s[12:13] offset:2304
	global_atomic_add v163, v197, s[12:13] offset:2560
	global_atomic_add v163, v197, s[12:13] offset:2816
	global_atomic_add v163, v197, s[12:13] offset:3072
	global_atomic_add v163, v197, s[12:13] offset:3328
	global_atomic_add v163, v197, s[12:13] offset:3584
	global_atomic_add v163, v197, s[12:13] offset:3840
	s_mov_b32 s5, 0
	global_load_dword v2, v163, s[18:19] sc1
	s_sleep 5
.Lbar_lead_poll_0:
	global_load_dword v3, v163, s[18:19] sc1
	s_waitcnt vmcnt(1)
	v_cmp_le_u32_e32 vcc, v16, v2
	s_cbranch_vccnz .Lbar_lead_done_0
	global_load_dword v2, v163, s[18:19] sc1
	s_waitcnt vmcnt(1)
	v_cmp_le_u32_e32 vcc, v16, v3
	s_cbranch_vccnz .Lbar_lead_done_0
	s_sleep 3
	s_add_i32 s5, s5, 1
	s_cmp_lt_u32 s5, 0x20000
	s_cbranch_scc1 .Lbar_lead_poll_0
.Lbar_lead_done_0:
	s_waitcnt vmcnt(0)
.LBB0_335:
	s_or_b64 exec, exec, s[0:1]
	s_waitcnt lgkmcnt(0)
	s_barrier

; __device__ __forceinline__ unsigned xb_ld(unsigned* p)              { return __hip_atomic_load(p, __ATOMIC_RELAXED, __HIP_MEMORY_SCOPE_AGENT); }
; __device__ __forceinline__ unsigned xb_add(unsigned* p, unsigned v) { return __hip_atomic_fetch_add(p, v, __ATOMIC_RELAXED, __HIP_MEMORY_SCOPE_AGENT); }
; #define XB_SPIN(cond, bar) do { unsigned _sp = 0; while (cond) { __builtin_amdgcn_s_sleep(1); \
;     if ((++_sp & 255u) == 0u) { if (xb_ld(&(bar)[XB_TMO])) break; if (_sp > XB_SPIN_CAP) { atomicAdd(&(bar)[XB_TMO], 1u); break; } } } } while (0)
; __device__ __forceinline__ void xcd_barrier(const XcdBarrier& b) {
;     ...
;             __builtin_amdgcn_fence(__ATOMIC_ACQUIRE, "agent");
;             xb_add(&bar[XB_XGEN(b.x)], 1u);
;             asm volatile("s_waitcnt vmcnt(0)" ::: "memory");
;         } else {
;             XB_SPIN(xb_ld(&bar[XB_XGEN(b.x)]) == gen, bar);
;             __builtin_amdgcn_fence(__ATOMIC_ACQUIRE, "agent");
;             asm volatile("s_waitcnt vmcnt(0)" ::: "memory");
;         }
;     }
;     __syncthreads();
.Lbar_lead_done_1:
	s_waitcnt vmcnt(0)
.LBB0_412:
	s_or_b64 exec, exec, s[0:1]
	s_waitcnt lgkmcnt(0)
	s_barrier

; __device__ __forceinline__ unsigned xb_ld(unsigned* p)              { return __hip_atomic_load(p, __ATOMIC_RELAXED, __HIP_MEMORY_SCOPE_AGENT); }
; __device__ __forceinline__ unsigned xb_add(unsigned* p, unsigned v) { return __hip_atomic_fetch_add(p, v, __ATOMIC_RELAXED, __HIP_MEMORY_SCOPE_AGENT); }
; #define XB_SPIN(cond, bar) do { unsigned _sp = 0; while (cond) { __builtin_amdgcn_s_sleep(1); \
;     if ((++_sp & 255u) == 0u) { if (xb_ld(&(bar)[XB_TMO])) break; if (_sp > XB_SPIN_CAP) { atomicAdd(&(bar)[XB_TMO], 1u); break; } } } } while (0)
; __device__ __forceinline__ void xcd_barrier(const XcdBarrier& b) {
;     ...
;             __builtin_amdgcn_fence(__ATOMIC_ACQUIRE, "agent");
;             xb_add(&bar[XB_XGEN(b.x)], 1u);
;             asm volatile("s_waitcnt vmcnt(0)" ::: "memory");
;         } else {
;             XB_SPIN(xb_ld(&bar[XB_XGEN(b.x)]) == gen, bar);
;             __builtin_amdgcn_fence(__ATOMIC_ACQUIRE, "agent");
;             asm volatile("s_waitcnt vmcnt(0)" ::: "memory");
;         }
;     }
;     __syncthreads();
.Lbar_lead_done_2:
	s_waitcnt vmcnt(0)
.LBB0_527:
	s_or_b64 exec, exec, s[0:1]
	s_waitcnt lgkmcnt(0)
	s_barrier

; __device__ __forceinline__ unsigned xb_ld(unsigned* p)              { return __hip_atomic_load(p, __ATOMIC_RELAXED, __HIP_MEMORY_SCOPE_AGENT); }
; __device__ __forceinline__ unsigned xb_add(unsigned* p, unsigned v) { return __hip_atomic_fetch_add(p, v, __ATOMIC_RELAXED, __HIP_MEMORY_SCOPE_AGENT); }
; #define XB_SPIN(cond, bar) do { unsigned _sp = 0; while (cond) { __builtin_amdgcn_s_sleep(1); \
;     if ((++_sp & 255u) == 0u) { if (xb_ld(&(bar)[XB_TMO])) break; if (_sp > XB_SPIN_CAP) { atomicAdd(&(bar)[XB_TMO], 1u); break; } } } } while (0)
; __device__ __forceinline__ void xcd_barrier(const XcdBarrier& b) {
;     ...
;             __builtin_amdgcn_fence(__ATOMIC_ACQUIRE, "agent");
;             xb_add(&bar[XB_XGEN(b.x)], 1u);
;             asm volatile("s_waitcnt vmcnt(0)" ::: "memory");
;         } else {
;             XB_SPIN(xb_ld(&bar[XB_XGEN(b.x)]) == gen, bar);
;             __builtin_amdgcn_fence(__ATOMIC_ACQUIRE, "agent");
;             asm volatile("s_waitcnt vmcnt(0)" ::: "memory");
;         }
;     }
;     __syncthreads();
.Lbar_lead_done_3:
	s_waitcnt vmcnt(0)
.LBB0_756:
	s_or_b64 exec, exec, s[0:1]
	s_waitcnt lgkmcnt(0)
	s_barrier

; __device__ __forceinline__ unsigned xb_ld(unsigned* p)              { return __hip_atomic_load(p, __ATOMIC_RELAXED, __HIP_MEMORY_SCOPE_AGENT); }
; __device__ __forceinline__ unsigned xb_add(unsigned* p, unsigned v) { return __hip_atomic_fetch_add(p, v, __ATOMIC_RELAXED, __HIP_MEMORY_SCOPE_AGENT); }
; #define XB_SPIN(cond, bar) do { unsigned _sp = 0; while (cond) { __builtin_amdgcn_s_sleep(1); \
;     if ((++_sp & 255u) == 0u) { if (xb_ld(&(bar)[XB_TMO])) break; if (_sp > XB_SPIN_CAP) { atomicAdd(&(bar)[XB_TMO], 1u); break; } } } } while (0)
; __device__ __forceinline__ void xcd_barrier(const XcdBarrier& b) {
;     ...
;             __builtin_amdgcn_fence(__ATOMIC_ACQUIRE, "agent");
;             xb_add(&bar[XB_XGEN(b.x)], 1u);
;             asm volatile("s_waitcnt vmcnt(0)" ::: "memory");
;         } else {
;             XB_SPIN(xb_ld(&bar[XB_XGEN(b.x)]) == gen, bar);
;             __builtin_amdgcn_fence(__ATOMIC_ACQUIRE, "agent");
;             asm volatile("s_waitcnt vmcnt(0)" ::: "memory");
;         }
;     }
;     __syncthreads();
.Lbar_lead_done_4:
	s_waitcnt vmcnt(0)
.LBB0_853:
	s_or_b64 exec, exec, s[0:1]
	s_waitcnt lgkmcnt(0)
	s_barrier

; __device__ __forceinline__ unsigned xb_ld(unsigned* p)              { return __hip_atomic_load(p, __ATOMIC_RELAXED, __HIP_MEMORY_SCOPE_AGENT); }
; __device__ __forceinline__ unsigned xb_add(unsigned* p, unsigned v) { return __hip_atomic_fetch_add(p, v, __ATOMIC_RELAXED, __HIP_MEMORY_SCOPE_AGENT); }
; #define XB_SPIN(cond, bar) do { unsigned _sp = 0; while (cond) { __builtin_amdgcn_s_sleep(1); \
;     if ((++_sp & 255u) == 0u) { if (xb_ld(&(bar)[XB_TMO])) break; if (_sp > XB_SPIN_CAP) { atomicAdd(&(bar)[XB_TMO], 1u); break; } } } } while (0)
; __device__ __forceinline__ void xcd_barrier(const XcdBarrier& b) {
;     ...
;             __builtin_amdgcn_fence(__ATOMIC_ACQUIRE, "agent");
;             xb_add(&bar[XB_XGEN(b.x)], 1u);
;             asm volatile("s_waitcnt vmcnt(0)" ::: "memory");
;         } else {
;             XB_SPIN(xb_ld(&bar[XB_XGEN(b.x)]) == gen, bar);
;             __builtin_amdgcn_fence(__ATOMIC_ACQUIRE, "agent");
;             asm volatile("s_waitcnt vmcnt(0)" ::: "memory");
;         }
;     }
;     __syncthreads();
.Lbar_lead_done_5:
	s_waitcnt vmcnt(0)
.LBB0_979:
	s_or_b64 exec, exec, s[0:1]
	s_waitcnt lgkmcnt(0)
	s_barrier

; __device__ __forceinline__ unsigned xb_ld(unsigned* p)              { return __hip_atomic_load(p, __ATOMIC_RELAXED, __HIP_MEMORY_SCOPE_AGENT); }
; __device__ __forceinline__ unsigned xb_add(unsigned* p, unsigned v) { return __hip_atomic_fetch_add(p, v, __ATOMIC_RELAXED, __HIP_MEMORY_SCOPE_AGENT); }
; #define XB_SPIN(cond, bar) do { unsigned _sp = 0; while (cond) { __builtin_amdgcn_s_sleep(1); \
;     if ((++_sp & 255u) == 0u) { if (xb_ld(&(bar)[XB_TMO])) break; if (_sp > XB_SPIN_CAP) { atomicAdd(&(bar)[XB_TMO], 1u); break; } } } } while (0)
; __device__ __forceinline__ void xcd_barrier(const XcdBarrier& b) {
;     ...
;             __builtin_amdgcn_fence(__ATOMIC_ACQUIRE, "agent");
;             xb_add(&bar[XB_XGEN(b.x)], 1u);
;             asm volatile("s_waitcnt vmcnt(0)" ::: "memory");
;         } else {
;             XB_SPIN(xb_ld(&bar[XB_XGEN(b.x)]) == gen, bar);
;             __builtin_amdgcn_fence(__ATOMIC_ACQUIRE, "agent");
;             asm volatile("s_waitcnt vmcnt(0)" ::: "memory");
;         }
;     }
;     __syncthreads();
.Lbar_lead_done_6:
	s_waitcnt vmcnt(0)
.LBB0_1039:
	s_or_b64 exec, exec, s[0:1]
	s_waitcnt lgkmcnt(0)
	s_barrier

; __device__ __forceinline__ unsigned xb_ld(unsigned* p)              { return __hip_atomic_load(p, __ATOMIC_RELAXED, __HIP_MEMORY_SCOPE_AGENT); }
; __device__ __forceinline__ unsigned xb_add(unsigned* p, unsigned v) { return __hip_atomic_fetch_add(p, v, __ATOMIC_RELAXED, __HIP_MEMORY_SCOPE_AGENT); }
; #define XB_SPIN(cond, bar) do { unsigned _sp = 0; while (cond) { __builtin_amdgcn_s_sleep(1); \
;     if ((++_sp & 255u) == 0u) { if (xb_ld(&(bar)[XB_TMO])) break; if (_sp > XB_SPIN_CAP) { atomicAdd(&(bar)[XB_TMO], 1u); break; } } } } while (0)
; __device__ __forceinline__ void xcd_barrier(const XcdBarrier& b) {
;     ...
;             __builtin_amdgcn_fence(__ATOMIC_ACQUIRE, "agent");
;             xb_add(&bar[XB_XGEN(b.x)], 1u);
;             asm volatile("s_waitcnt vmcnt(0)" ::: "memory");
;         } else {
;             XB_SPIN(xb_ld(&bar[XB_XGEN(b.x)]) == gen, bar);
;             __builtin_amdgcn_fence(__ATOMIC_ACQUIRE, "agent");
;             asm volatile("s_waitcnt vmcnt(0)" ::: "memory");
;         }
;     }
;     __syncthreads();
.Lbar_lead_done_7:
	s_waitcnt vmcnt(0)
.LBB0_1116:
	s_or_b64 exec, exec, s[0:1]
	s_waitcnt lgkmcnt(0)
	s_barrier

; __device__ __forceinline__ unsigned xb_ld(unsigned* p)              { return __hip_atomic_load(p, __ATOMIC_RELAXED, __HIP_MEMORY_SCOPE_AGENT); }
; __device__ __forceinline__ unsigned xb_add(unsigned* p, unsigned v) { return __hip_atomic_fetch_add(p, v, __ATOMIC_RELAXED, __HIP_MEMORY_SCOPE_AGENT); }
; #define XB_SPIN(cond, bar) do { unsigned _sp = 0; while (cond) { __builtin_amdgcn_s_sleep(1); \
;     if ((++_sp & 255u) == 0u) { if (xb_ld(&(bar)[XB_TMO])) break; if (_sp > XB_SPIN_CAP) { atomicAdd(&(bar)[XB_TMO], 1u); break; } } } } while (0)
; __device__ __forceinline__ void xcd_barrier(const XcdBarrier& b) {
;     ...
;             __builtin_amdgcn_fence(__ATOMIC_ACQUIRE, "agent");
;             xb_add(&bar[XB_XGEN(b.x)], 1u);
;             asm volatile("s_waitcnt vmcnt(0)" ::: "memory");
;         } else {
;             XB_SPIN(xb_ld(&bar[XB_XGEN(b.x)]) == gen, bar);
;             __builtin_amdgcn_fence(__ATOMIC_ACQUIRE, "agent");
;             asm volatile("s_waitcnt vmcnt(0)" ::: "memory");
;         }
;     }
;     __syncthreads();
.Lbar_lead_done_8:
	s_waitcnt vmcnt(0)
.LBB0_1192:
	s_or_b64 exec, exec, s[0:1]
	s_waitcnt lgkmcnt(0)
	s_barrier

; __device__ __forceinline__ unsigned xb_ld(unsigned* p)              { return __hip_atomic_load(p, __ATOMIC_RELAXED, __HIP_MEMORY_SCOPE_AGENT); }
; __device__ __forceinline__ unsigned xb_add(unsigned* p, unsigned v) { return __hip_atomic_fetch_add(p, v, __ATOMIC_RELAXED, __HIP_MEMORY_SCOPE_AGENT); }
; #define XB_SPIN(cond, bar) do { unsigned _sp = 0; while (cond) { __builtin_amdgcn_s_sleep(1); \
;     if ((++_sp & 255u) == 0u) { if (xb_ld(&(bar)[XB_TMO])) break; if (_sp > XB_SPIN_CAP) { atomicAdd(&(bar)[XB_TMO], 1u); break; } } } } while (0)
; __device__ __forceinline__ void xcd_barrier(const XcdBarrier& b) {
;     ...
;             __builtin_amdgcn_fence(__ATOMIC_ACQUIRE, "agent");
;             xb_add(&bar[XB_XGEN(b.x)], 1u);
;             asm volatile("s_waitcnt vmcnt(0)" ::: "memory");
;         } else {
;             XB_SPIN(xb_ld(&bar[XB_XGEN(b.x)]) == gen, bar);
;             __builtin_amdgcn_fence(__ATOMIC_ACQUIRE, "agent");
;             asm volatile("s_waitcnt vmcnt(0)" ::: "memory");
;         }
;     }
;     __syncthreads();
.Lbar_lead_done_9:
	s_waitcnt vmcnt(0)
.LBB0_1314:
	s_or_b64 exec, exec, s[0:1]
	s_waitcnt lgkmcnt(0)
	s_barrier

; __device__ __forceinline__ unsigned xb_ld(unsigned* p)              { return __hip_atomic_load(p, __ATOMIC_RELAXED, __HIP_MEMORY_SCOPE_AGENT); }
; __device__ __forceinline__ unsigned xb_add(unsigned* p, unsigned v) { return __hip_atomic_fetch_add(p, v, __ATOMIC_RELAXED, __HIP_MEMORY_SCOPE_AGENT); }
; #define XB_SPIN(cond, bar) do { unsigned _sp = 0; while (cond) { __builtin_amdgcn_s_sleep(1); \
;     if ((++_sp & 255u) == 0u) { if (xb_ld(&(bar)[XB_TMO])) break; if (_sp > XB_SPIN_CAP) { atomicAdd(&(bar)[XB_TMO], 1u); break; } } } } while (0)
; __device__ __forceinline__ void xcd_barrier(const XcdBarrier& b) {
;     ...
;             __builtin_amdgcn_fence(__ATOMIC_ACQUIRE, "agent");
;             xb_add(&bar[XB_XGEN(b.x)], 1u);
;             asm volatile("s_waitcnt vmcnt(0)" ::: "memory");
;         } else {
;             XB_SPIN(xb_ld(&bar[XB_XGEN(b.x)]) == gen, bar);
;             __builtin_amdgcn_fence(__ATOMIC_ACQUIRE, "agent");
;             asm volatile("s_waitcnt vmcnt(0)" ::: "memory");
;         }
;     }
;     __syncthreads();
.Lbar_lead_done_10:
	s_waitcnt vmcnt(0)
.LBB0_1435:
	s_or_b64 exec, exec, s[0:1]
	s_waitcnt lgkmcnt(0)
	s_barrier

; __device__ __forceinline__ unsigned xb_ld(unsigned* p)              { return __hip_atomic_load(p, __ATOMIC_RELAXED, __HIP_MEMORY_SCOPE_AGENT); }
; __device__ __forceinline__ unsigned xb_add(unsigned* p, unsigned v) { return __hip_atomic_fetch_add(p, v, __ATOMIC_RELAXED, __HIP_MEMORY_SCOPE_AGENT); }
; #define XB_SPIN(cond, bar) do { unsigned _sp = 0; while (cond) { __builtin_amdgcn_s_sleep(1); \
;     if ((++_sp & 255u) == 0u) { if (xb_ld(&(bar)[XB_TMO])) break; if (_sp > XB_SPIN_CAP) { atomicAdd(&(bar)[XB_TMO], 1u); break; } } } } while (0)
; __device__ __forceinline__ void xcd_barrier(const XcdBarrier& b) {
;     ...
;             __builtin_amdgcn_fence(__ATOMIC_ACQUIRE, "agent");
;             xb_add(&bar[XB_XGEN(b.x)], 1u);
;             asm volatile("s_waitcnt vmcnt(0)" ::: "memory");
;         } else {
;             XB_SPIN(xb_ld(&bar[XB_XGEN(b.x)]) == gen, bar);
;             __builtin_amdgcn_fence(__ATOMIC_ACQUIRE, "agent");
;             asm volatile("s_waitcnt vmcnt(0)" ::: "memory");
;         }
;     }
;     __syncthreads();
.Lbar_lead_done_11:
	s_waitcnt vmcnt(0)
.LBB0_1497:
	s_or_b64 exec, exec, s[0:1]
	s_waitcnt lgkmcnt(0)
	s_barrier

; __device__ __forceinline__ unsigned xb_ld(unsigned* p)              { return __hip_atomic_load(p, __ATOMIC_RELAXED, __HIP_MEMORY_SCOPE_AGENT); }
; __device__ __forceinline__ unsigned xb_add(unsigned* p, unsigned v) { return __hip_atomic_fetch_add(p, v, __ATOMIC_RELAXED, __HIP_MEMORY_SCOPE_AGENT); }
; #define XB_SPIN(cond, bar) do { unsigned _sp = 0; while (cond) { __builtin_amdgcn_s_sleep(1); \
;     if ((++_sp & 255u) == 0u) { if (xb_ld(&(bar)[XB_TMO])) break; if (_sp > XB_SPIN_CAP) { atomicAdd(&(bar)[XB_TMO], 1u); break; } } } } while (0)
; __device__ __forceinline__ void xcd_barrier(const XcdBarrier& b) {
;     ...
;         if (old + 1u == (gen + 1u) * nloc) {
;             __builtin_amdgcn_fence(__ATOMIC_RELEASE, "agent");
;             asm volatile("s_waitcnt vmcnt(0)" ::: "memory");
;             const unsigned og = xb_add(&bar[XB_TOP], 1u);
;             const unsigned tg = og / nx;
;             if (og + 1u == (tg + 1u) * nx) xb_add(&bar[XB_TOPGEN], 1u);
;             else XB_SPIN(xb_ld(&bar[XB_TOPGEN]) == tg, bar);
.LBB0_1553:
	s_mov_b64 s[6:7], exec
	buffer_wbl2 sc1
	v_readlane_b32 s18, v253, 48
	v_readlane_b32 s19, v253, 49
	v_readlane_b32 s12, v253, 52
	v_readlane_b32 s13, v253, 53
	s_nop 3
	s_add_u32 s18, s18, 0x3600
	s_addc_u32 s19, s19, 0
	s_add_u32 s12, s12, 0x2500
	s_addc_u32 s13, s13, 0
	s_waitcnt lgkmcnt(0)
	s_waitcnt vmcnt(0)
	global_atomic_add v163, v197, s[12:13]
	global_atomic_add v163, v197, s[12:13] offset:256
	global_atomic_add v163, v197, s[12:13] offset:512
	global_atomic_add v163, v197, s[12:13] offset:768
	global_atomic_add v163, v197, s[12:13] offset:1024
	global_atomic_add v163, v197, s[12:13] offset:1280
	global_atomic_add v163, v197, s[12:13] offset:1536
	global_atomic_add v163, v197, s[12:13] offset:1792
	global_atomic_add v163, v197, s[12:13] offset:2048
	global_atomic_add v163, v197, s[12:13] offset:2304
	global_atomic_add v163, v197, s[12:13] offset:2560
	global_atomic_add v163, v197, s[12:13] offset:2816
	global_atomic_add v163, v197, s[12:13] offset:3072
	global_atomic_add v163, v197, s[12:13] offset:3328
	global_atomic_add v163, v197, s[12:13] offset:3584
	global_atomic_add v163, v197, s[12:13] offset:3840
	s_mov_b32 s5, 0
	global_load_dword v2, v163, s[18:19] sc1
	s_sleep 5

; __device__ __forceinline__ unsigned xb_ld(unsigned* p)              { return __hip_atomic_load(p, __ATOMIC_RELAXED, __HIP_MEMORY_SCOPE_AGENT); }
; __device__ __forceinline__ unsigned xb_add(unsigned* p, unsigned v) { return __hip_atomic_fetch_add(p, v, __ATOMIC_RELAXED, __HIP_MEMORY_SCOPE_AGENT); }
; #define XB_SPIN(cond, bar) do { unsigned _sp = 0; while (cond) { __builtin_amdgcn_s_sleep(1); \
;     if ((++_sp & 255u) == 0u) { if (xb_ld(&(bar)[XB_TMO])) break; if (_sp > XB_SPIN_CAP) { atomicAdd(&(bar)[XB_TMO], 1u); break; } } } } while (0)
; __device__ __forceinline__ void xcd_barrier(const XcdBarrier& b) {
;     ...
;             __builtin_amdgcn_fence(__ATOMIC_ACQUIRE, "agent");
;             xb_add(&bar[XB_XGEN(b.x)], 1u);
;             asm volatile("s_waitcnt vmcnt(0)" ::: "memory");
;         } else {
;             XB_SPIN(xb_ld(&bar[XB_XGEN(b.x)]) == gen, bar);
;             __builtin_amdgcn_fence(__ATOMIC_ACQUIRE, "agent");
;             asm volatile("s_waitcnt vmcnt(0)" ::: "memory");
;         }
;     }
;     __syncthreads();
.Lbar_lead_done_12:
	s_waitcnt vmcnt(0)
	s_mov_b64 s[8:9], 0
	s_getpc_b64 s[98:99]
